# v52 + MoE weight conversion: exact x32 scale folded into the fp8 conversion (v_cvt_scalef32_pk_fp8_f32, scale 2^-5), 128 v_mul removed per item-wave; same fp8 results
# speedup vs baseline: 1.0122x; 1.0122x over previous
.LBB0_249:
	s_lshl_b32 s42, s62, 16
	s_add_i32 s65, s42, 0
	v_add_u32_e32 v0, s65, v134
	v_add_u32_e32 v157, v0, v136
	v_add_u32_e32 v156, v0, v137
	s_waitcnt vmcnt(24)
	v_mov_b32_e32 v162, 0x3d000000
	v_cvt_scalef32_pk_fp8_f32 v158, v120, v116, v162
	v_cvt_scalef32_pk_fp8_f32 v159, v112, v100, v162
	v_cvt_scalef32_pk_fp8_f32 v160, v96, v84, v162
	v_cvt_scalef32_pk_fp8_f32 v161, v80, v68, v162
	v_cvt_scalef32_pk_fp8_f32 v158, v124, v108, v162 op_sel:[0,0,0,1]
	v_cvt_scalef32_pk_fp8_f32 v159, v104, v92, v162 op_sel:[0,0,0,1]
	v_cvt_scalef32_pk_fp8_f32 v160, v88, v76, v162 op_sel:[0,0,0,1]
	v_cvt_scalef32_pk_fp8_f32 v161, v72, v60, v162 op_sel:[0,0,0,1]
	ds_write_b128 v157, v[158:161]
	v_mov_b32_e32 v162, 0x3d000000
	v_cvt_scalef32_pk_fp8_f32 v168, v121, v117, v162
	v_cvt_scalef32_pk_fp8_f32 v169, v113, v101, v162
	v_cvt_scalef32_pk_fp8_f32 v170, v97, v85, v162
	v_cvt_scalef32_pk_fp8_f32 v171, v81, v69, v162
	v_cvt_scalef32_pk_fp8_f32 v168, v125, v109, v162 op_sel:[0,0,0,1]
	v_cvt_scalef32_pk_fp8_f32 v169, v105, v93, v162 op_sel:[0,0,0,1]
	v_cvt_scalef32_pk_fp8_f32 v170, v89, v77, v162 op_sel:[0,0,0,1]
	v_cvt_scalef32_pk_fp8_f32 v171, v73, v61, v162 op_sel:[0,0,0,1]
	ds_write_b128 v157, v[168:171] offset:256
	v_mov_b32_e32 v162, 0x3d000000
	v_cvt_scalef32_pk_fp8_f32 v158, v122, v118, v162
	v_cvt_scalef32_pk_fp8_f32 v159, v114, v102, v162
	v_cvt_scalef32_pk_fp8_f32 v160, v98, v86, v162
	v_cvt_scalef32_pk_fp8_f32 v161, v82, v70, v162
	v_cvt_scalef32_pk_fp8_f32 v158, v126, v110, v162 op_sel:[0,0,0,1]
	v_cvt_scalef32_pk_fp8_f32 v159, v106, v94, v162 op_sel:[0,0,0,1]
	v_cvt_scalef32_pk_fp8_f32 v160, v90, v78, v162 op_sel:[0,0,0,1]
	v_cvt_scalef32_pk_fp8_f32 v161, v74, v62, v162 op_sel:[0,0,0,1]
	ds_write_b128 v157, v[158:161] offset:512
	v_mov_b32_e32 v162, 0x3d000000
	v_cvt_scalef32_pk_fp8_f32 v168, v123, v119, v162
	v_cvt_scalef32_pk_fp8_f32 v169, v115, v103, v162
	v_cvt_scalef32_pk_fp8_f32 v170, v99, v87, v162
	v_cvt_scalef32_pk_fp8_f32 v171, v83, v71, v162
	v_cvt_scalef32_pk_fp8_f32 v168, v127, v111, v162 op_sel:[0,0,0,1]
	v_cvt_scalef32_pk_fp8_f32 v169, v107, v95, v162 op_sel:[0,0,0,1]
	v_cvt_scalef32_pk_fp8_f32 v170, v91, v79, v162 op_sel:[0,0,0,1]
	v_cvt_scalef32_pk_fp8_f32 v171, v75, v63, v162 op_sel:[0,0,0,1]
	ds_write_b128 v157, v[168:171] offset:768
	s_add_i32 s63, s63, s33
	s_cmpk_gt_i32 s63, 0x17ff
	s_cselect_b64 s[54:55], -1, 0
	s_and_b64 vcc, exec, s[54:55]
	s_mov_b32 s56, s66
	s_cbranch_vccnz .Lcv_nonext
	s_cmpk_gt_i32 s63, 0xfff
	s_mov_b64 s[60:61], -1
	s_cbranch_scc0 .LBB0_252
	s_add_i32 s14, s63, 0xfffff000
	s_lshr_b32 s42, s14, 6
	s_lshl_b64 s[14:15], s[42:43], 22
	s_lshl_b64 s[56:57], s[42:43], 24
	s_add_u32 s58, s24, s56
	s_addc_u32 s59, s25, s57
	s_add_u32 s14, s16, s14
	s_addc_u32 s15, s17, s15
	s_and_b32 s64, s10, 0x700
	s_and_b32 s56, s44, 0x700
	s_mov_b64 s[60:61], 0

.LBB0_247:
	s_add_i32 s42, s64, s69
	s_mul_hi_i32 s71, s60, s42
	s_mul_i32 s70, s60, s42
	s_lshl_b64 s[70:71], s[70:71], 2
	s_add_u32 s42, s58, s70
	s_addc_u32 s70, s59, s71
	s_ashr_i32 s57, s56, 31
	s_lshl_b64 s[58:59], s[56:57], 2
	s_add_u32 s58, s42, s58
	s_addc_u32 s59, s70, s59
	s_lshl_b32 s42, s60, 2
	v_lshlrev_b32_e32 v166, 2, v132
	global_load_dwordx4 v[120:123], v166, s[58:59] nt
	s_add_u32 s58, s58, s42
	s_addc_u32 s59, s59, 0
	global_load_dwordx4 v[116:119], v166, s[58:59] nt
	s_add_u32 s58, s58, s42
	s_addc_u32 s59, s59, 0
	global_load_dwordx4 v[124:127], v166, s[58:59] nt
	s_add_u32 s58, s58, s42
	s_addc_u32 s59, s59, 0
	global_load_dwordx4 v[108:111], v166, s[58:59] nt
	s_add_u32 s58, s58, s42
	s_addc_u32 s59, s59, 0
	global_load_dwordx4 v[112:115], v166, s[58:59] nt
	s_add_u32 s58, s58, s42
	s_addc_u32 s59, s59, 0
	global_load_dwordx4 v[100:103], v166, s[58:59] nt
	s_add_u32 s58, s58, s42
	s_addc_u32 s59, s59, 0
	global_load_dwordx4 v[104:107], v166, s[58:59] nt
	s_add_u32 s58, s58, s42
	s_addc_u32 s59, s59, 0
	global_load_dwordx4 v[92:95], v166, s[58:59] nt
	s_add_u32 s58, s58, s42
	s_addc_u32 s59, s59, 0
	global_load_dwordx4 v[96:99], v166, s[58:59] nt
	s_add_u32 s58, s58, s42
	s_addc_u32 s59, s59, 0
	global_load_dwordx4 v[84:87], v166, s[58:59] nt
	s_add_u32 s58, s58, s42
	s_addc_u32 s59, s59, 0
	global_load_dwordx4 v[88:91], v166, s[58:59] nt
	s_add_u32 s58, s58, s42
	s_addc_u32 s59, s59, 0
	global_load_dwordx4 v[76:79], v166, s[58:59] nt
	s_add_u32 s58, s58, s42
	s_addc_u32 s59, s59, 0
	global_load_dwordx4 v[80:83], v166, s[58:59] nt
	s_add_u32 s58, s58, s42
	s_addc_u32 s59, s59, 0
	global_load_dwordx4 v[68:71], v166, s[58:59] nt
	s_add_u32 s58, s58, s42
	s_addc_u32 s59, s59, 0
	global_load_dwordx4 v[72:75], v166, s[58:59] nt
	s_add_u32 s58, s58, s42
	s_addc_u32 s59, s59, 0
	global_load_dwordx4 v[60:63], v166, s[58:59] nt
	s_add_u32 s58, s58, s42
	s_addc_u32 s59, s59, 0
	s_waitcnt vmcnt(24)
	v_mov_b32_e32 v162, 0x3d000000
	v_cvt_scalef32_pk_fp8_f32 v158, v64, v52, v162
	v_cvt_scalef32_pk_fp8_f32 v159, v48, v36, v162
	v_cvt_scalef32_pk_fp8_f32 v160, v32, v20, v162
	v_cvt_scalef32_pk_fp8_f32 v161, v16, v4, v162
	v_cvt_scalef32_pk_fp8_f32 v158, v56, v44, v162 op_sel:[0,0,0,1]
	v_cvt_scalef32_pk_fp8_f32 v159, v40, v28, v162 op_sel:[0,0,0,1]
	v_cvt_scalef32_pk_fp8_f32 v160, v24, v12, v162 op_sel:[0,0,0,1]
	v_cvt_scalef32_pk_fp8_f32 v161, v8, v128, v162 op_sel:[0,0,0,1]
	ds_write_b128 v156, v[158:161]
	v_mov_b32_e32 v162, 0x3d000000
	v_cvt_scalef32_pk_fp8_f32 v168, v65, v53, v162
	v_cvt_scalef32_pk_fp8_f32 v169, v49, v37, v162
	v_cvt_scalef32_pk_fp8_f32 v170, v33, v21, v162
	v_cvt_scalef32_pk_fp8_f32 v171, v17, v5, v162
	v_cvt_scalef32_pk_fp8_f32 v168, v57, v45, v162 op_sel:[0,0,0,1]
	v_cvt_scalef32_pk_fp8_f32 v169, v41, v29, v162 op_sel:[0,0,0,1]
	v_cvt_scalef32_pk_fp8_f32 v170, v25, v13, v162 op_sel:[0,0,0,1]
	v_cvt_scalef32_pk_fp8_f32 v171, v9, v129, v162 op_sel:[0,0,0,1]
	ds_write_b128 v156, v[168:171] offset:256
	v_mov_b32_e32 v162, 0x3d000000
	v_cvt_scalef32_pk_fp8_f32 v158, v66, v54, v162
	v_cvt_scalef32_pk_fp8_f32 v159, v50, v38, v162
	v_cvt_scalef32_pk_fp8_f32 v160, v34, v22, v162
	v_cvt_scalef32_pk_fp8_f32 v161, v18, v6, v162
	v_cvt_scalef32_pk_fp8_f32 v158, v58, v46, v162 op_sel:[0,0,0,1]
	v_cvt_scalef32_pk_fp8_f32 v159, v42, v30, v162 op_sel:[0,0,0,1]
	v_cvt_scalef32_pk_fp8_f32 v160, v26, v14, v162 op_sel:[0,0,0,1]
	v_cvt_scalef32_pk_fp8_f32 v161, v10, v130, v162 op_sel:[0,0,0,1]
	ds_write_b128 v156, v[158:161] offset:512
	v_mov_b32_e32 v162, 0x3d000000
	v_cvt_scalef32_pk_fp8_f32 v168, v67, v55, v162
	v_cvt_scalef32_pk_fp8_f32 v169, v51, v39, v162
	v_cvt_scalef32_pk_fp8_f32 v170, v35, v23, v162
	v_cvt_scalef32_pk_fp8_f32 v171, v19, v7, v162
	v_cvt_scalef32_pk_fp8_f32 v168, v59, v47, v162 op_sel:[0,0,0,1]
	v_cvt_scalef32_pk_fp8_f32 v169, v43, v31, v162 op_sel:[0,0,0,1]
	v_cvt_scalef32_pk_fp8_f32 v170, v27, v15, v162 op_sel:[0,0,0,1]
	v_cvt_scalef32_pk_fp8_f32 v171, v11, v131, v162 op_sel:[0,0,0,1]
	ds_write_b128 v156, v[168:171] offset:768
	global_load_dwordx4 v[64:67], v166, s[58:59] nt
	s_add_u32 s58, s58, s42
	s_addc_u32 s59, s59, 0
	global_load_dwordx4 v[52:55], v166, s[58:59] nt
	s_add_u32 s58, s58, s42
	s_addc_u32 s59, s59, 0
	global_load_dwordx4 v[56:59], v166, s[58:59] nt
	s_add_u32 s58, s58, s42
	s_addc_u32 s59, s59, 0
	global_load_dwordx4 v[44:47], v166, s[58:59] nt
	s_add_u32 s58, s58, s42
	s_addc_u32 s59, s59, 0
	global_load_dwordx4 v[48:51], v166, s[58:59] nt
	s_add_u32 s58, s58, s42
	s_addc_u32 s59, s59, 0
	global_load_dwordx4 v[36:39], v166, s[58:59] nt
	s_add_u32 s58, s58, s42
	s_addc_u32 s59, s59, 0
	global_load_dwordx4 v[40:43], v166, s[58:59] nt
	s_add_u32 s58, s58, s42
	s_addc_u32 s59, s59, 0
	global_load_dwordx4 v[28:31], v166, s[58:59] nt
	s_add_u32 s58, s58, s42
	s_addc_u32 s59, s59, 0
	global_load_dwordx4 v[32:35], v166, s[58:59] nt
	s_add_u32 s58, s58, s42
	s_addc_u32 s59, s59, 0
	global_load_dwordx4 v[20:23], v166, s[58:59] nt
	s_add_u32 s58, s58, s42
	s_addc_u32 s59, s59, 0
	global_load_dwordx4 v[24:27], v166, s[58:59] nt
	s_add_u32 s58, s58, s42
	s_addc_u32 s59, s59, 0
	global_load_dwordx4 v[12:15], v166, s[58:59] nt
	s_add_u32 s58, s58, s42
	s_addc_u32 s59, s59, 0
	global_load_dwordx4 v[16:19], v166, s[58:59] nt
	s_add_u32 s58, s58, s42
	s_addc_u32 s59, s59, 0
	global_load_dwordx4 v[4:7], v166, s[58:59] nt
	s_add_u32 s58, s58, s42
	s_addc_u32 s59, s59, 0
	global_load_dwordx4 v[8:11], v166, s[58:59] nt
	s_add_u32 s58, s58, s42
	s_addc_u32 s59, s59, 0
	global_load_dwordx4 v[128:131], v166, s[58:59] nt
	s_add_u32 s58, s58, s42
	s_addc_u32 s59, s59, 0
	v_mov_b32_e32 v154, s61
	s_branch .Lcv_join
.Lcv_nonext:
	s_waitcnt vmcnt(8)
	v_mov_b32_e32 v162, 0x3d000000
	v_cvt_scalef32_pk_fp8_f32 v158, v64, v52, v162
	v_cvt_scalef32_pk_fp8_f32 v159, v48, v36, v162
	v_cvt_scalef32_pk_fp8_f32 v160, v32, v20, v162
	v_cvt_scalef32_pk_fp8_f32 v161, v16, v4, v162
	v_cvt_scalef32_pk_fp8_f32 v158, v56, v44, v162 op_sel:[0,0,0,1]
	v_cvt_scalef32_pk_fp8_f32 v159, v40, v28, v162 op_sel:[0,0,0,1]
	v_cvt_scalef32_pk_fp8_f32 v160, v24, v12, v162 op_sel:[0,0,0,1]
	v_cvt_scalef32_pk_fp8_f32 v161, v8, v128, v162 op_sel:[0,0,0,1]
	ds_write_b128 v156, v[158:161]
	v_mov_b32_e32 v162, 0x3d000000
	v_cvt_scalef32_pk_fp8_f32 v168, v65, v53, v162
	v_cvt_scalef32_pk_fp8_f32 v169, v49, v37, v162
	v_cvt_scalef32_pk_fp8_f32 v170, v33, v21, v162
	v_cvt_scalef32_pk_fp8_f32 v171, v17, v5, v162
	v_cvt_scalef32_pk_fp8_f32 v168, v57, v45, v162 op_sel:[0,0,0,1]
	v_cvt_scalef32_pk_fp8_f32 v169, v41, v29, v162 op_sel:[0,0,0,1]
	v_cvt_scalef32_pk_fp8_f32 v170, v25, v13, v162 op_sel:[0,0,0,1]
	v_cvt_scalef32_pk_fp8_f32 v171, v9, v129, v162 op_sel:[0,0,0,1]
	ds_write_b128 v156, v[168:171] offset:256
	v_mov_b32_e32 v162, 0x3d000000
	v_cvt_scalef32_pk_fp8_f32 v158, v66, v54, v162
	v_cvt_scalef32_pk_fp8_f32 v159, v50, v38, v162
	v_cvt_scalef32_pk_fp8_f32 v160, v34, v22, v162
	v_cvt_scalef32_pk_fp8_f32 v161, v18, v6, v162
	v_cvt_scalef32_pk_fp8_f32 v158, v58, v46, v162 op_sel:[0,0,0,1]
	v_cvt_scalef32_pk_fp8_f32 v159, v42, v30, v162 op_sel:[0,0,0,1]
	v_cvt_scalef32_pk_fp8_f32 v160, v26, v14, v162 op_sel:[0,0,0,1]
	v_cvt_scalef32_pk_fp8_f32 v161, v10, v130, v162 op_sel:[0,0,0,1]
	ds_write_b128 v156, v[158:161] offset:512
	v_mov_b32_e32 v162, 0x3d000000
	v_cvt_scalef32_pk_fp8_f32 v168, v67, v55, v162
	v_cvt_scalef32_pk_fp8_f32 v169, v51, v39, v162
	v_cvt_scalef32_pk_fp8_f32 v170, v35, v23, v162
	v_cvt_scalef32_pk_fp8_f32 v171, v19, v7, v162
	v_cvt_scalef32_pk_fp8_f32 v168, v59, v47, v162 op_sel:[0,0,0,1]
	v_cvt_scalef32_pk_fp8_f32 v169, v43, v31, v162 op_sel:[0,0,0,1]
	v_cvt_scalef32_pk_fp8_f32 v170, v27, v15, v162 op_sel:[0,0,0,1]
	v_cvt_scalef32_pk_fp8_f32 v171, v11, v131, v162 op_sel:[0,0,0,1]
	ds_write_b128 v156, v[168:171] offset:768
